# v12 + dropped five vmcnt(0) waits at GEMM unit / prologue accumulator zeroing (they only covered loads that are long complete; the K-loop's counted waits cover the staged tiles)
# speedup vs baseline: 1.0034x; 1.0034x over previous
.LBB0_106:
	s_add_u32 s24, s22, 0xf00
	s_addc_u32 s25, s23, 0
	s_and_b64 s[20:21], s[20:21], exec
	ds_write_b128 v195, v[0:3]
	s_cselect_b32 s20, s18, s24
	s_cselect_b32 s21, s19, s25
	s_add_u32 s51, s22, 0x100
	v_mov_b32_e32 v0, 0
	s_addc_u32 s52, s23, 0
	s_mov_b32 s53, -2
	s_mov_b64 s[22:23], 0
	v_mov_b32_e32 v1, v0
	v_mov_b32_e32 v2, v0
	v_mov_b32_e32 v3, v0
	v_mov_b32_e32 v4, v0
	v_mov_b32_e32 v5, v0
	v_mov_b32_e32 v6, v0
	v_mov_b32_e32 v7, v0
	v_mov_b32_e32 v16, v0
	v_mov_b32_e32 v17, v0
	v_mov_b32_e32 v18, v0
	v_mov_b32_e32 v19, v0
	v_mov_b32_e32 v20, v0
	v_mov_b32_e32 v21, v0
	v_mov_b32_e32 v22, v0
	v_mov_b32_e32 v23, v0
	v_mov_b32_e32 v32, v0
	v_mov_b32_e32 v33, v0
	v_mov_b32_e32 v34, v0
	v_mov_b32_e32 v35, v0
	v_mov_b32_e32 v36, v0
	v_mov_b32_e32 v37, v0
	v_mov_b32_e32 v38, v0
	v_mov_b32_e32 v39, v0
	v_mov_b32_e32 v48, v0
	v_mov_b32_e32 v49, v0
	v_mov_b32_e32 v50, v0
	v_mov_b32_e32 v51, v0
	v_mov_b32_e32 v52, v0
	v_mov_b32_e32 v53, v0
	v_mov_b32_e32 v54, v0
	v_mov_b32_e32 v55, v0
	v_mov_b32_e32 v8, v0
	v_mov_b32_e32 v9, v0
	v_mov_b32_e32 v10, v0
	v_mov_b32_e32 v11, v0
	v_mov_b32_e32 v12, v0
	v_mov_b32_e32 v13, v0
	v_mov_b32_e32 v14, v0
	v_mov_b32_e32 v15, v0
	v_mov_b32_e32 v24, v0
	v_mov_b32_e32 v25, v0
	v_mov_b32_e32 v26, v0
	v_mov_b32_e32 v27, v0
	v_mov_b32_e32 v28, v0
	v_mov_b32_e32 v29, v0
	v_mov_b32_e32 v30, v0
	v_mov_b32_e32 v31, v0
	v_mov_b32_e32 v40, v0
	v_mov_b32_e32 v41, v0
	v_mov_b32_e32 v42, v0
	v_mov_b32_e32 v43, v0
	v_mov_b32_e32 v44, v0
	v_mov_b32_e32 v45, v0
	v_mov_b32_e32 v46, v0
	v_mov_b32_e32 v47, v0
	v_mov_b32_e32 v56, v0
	v_mov_b32_e32 v57, v0
	v_mov_b32_e32 v58, v0
	v_mov_b32_e32 v59, v0
	v_mov_b32_e32 v60, v0
	v_mov_b32_e32 v61, v0
	v_mov_b32_e32 v62, v0
	v_mov_b32_e32 v63, v0
	v_mov_b32_e32 v68, v0
	v_mov_b32_e32 v69, v0
	v_mov_b32_e32 v70, v0
	v_mov_b32_e32 v71, v0
	v_mov_b32_e32 v72, v0
	v_mov_b32_e32 v73, v0
	v_mov_b32_e32 v74, v0
	v_mov_b32_e32 v75, v0
	v_mov_b32_e32 v84, v0
	v_mov_b32_e32 v85, v0
	v_mov_b32_e32 v86, v0
	v_mov_b32_e32 v87, v0
	v_mov_b32_e32 v88, v0
	v_mov_b32_e32 v89, v0
	v_mov_b32_e32 v90, v0
	v_mov_b32_e32 v91, v0
	v_mov_b32_e32 v100, v0
	v_mov_b32_e32 v101, v0
	v_mov_b32_e32 v102, v0
	v_mov_b32_e32 v103, v0
	v_mov_b32_e32 v104, v0
	v_mov_b32_e32 v105, v0
	v_mov_b32_e32 v106, v0
	v_mov_b32_e32 v107, v0
	v_mov_b32_e32 v116, v0
	v_mov_b32_e32 v117, v0
	v_mov_b32_e32 v118, v0
	v_mov_b32_e32 v119, v0
	v_mov_b32_e32 v120, v0
	v_mov_b32_e32 v121, v0
	v_mov_b32_e32 v122, v0
	v_mov_b32_e32 v123, v0
	v_mov_b32_e32 v76, v0
	v_mov_b32_e32 v77, v0
	v_mov_b32_e32 v78, v0
	v_mov_b32_e32 v79, v0
	v_mov_b32_e32 v80, v0
	v_mov_b32_e32 v81, v0
	v_mov_b32_e32 v82, v0
	v_mov_b32_e32 v83, v0
	v_mov_b32_e32 v92, v0
	v_mov_b32_e32 v93, v0
	v_mov_b32_e32 v94, v0
	v_mov_b32_e32 v95, v0
	v_mov_b32_e32 v96, v0
	v_mov_b32_e32 v97, v0
	v_mov_b32_e32 v98, v0
	v_mov_b32_e32 v99, v0
	v_mov_b32_e32 v108, v0
	v_mov_b32_e32 v109, v0
	v_mov_b32_e32 v110, v0
	v_mov_b32_e32 v111, v0
	v_mov_b32_e32 v112, v0
	v_mov_b32_e32 v113, v0
	v_mov_b32_e32 v114, v0
	v_mov_b32_e32 v115, v0
	v_mov_b32_e32 v124, v0
	v_mov_b32_e32 v125, v0
	v_mov_b32_e32 v126, v0
	v_mov_b32_e32 v127, v0
	v_mov_b32_e32 v128, v0
	v_mov_b32_e32 v129, v0
	v_mov_b32_e32 v130, v0
	v_mov_b32_e32 v131, v0
	s_branch .LBB0_108

.LBB0_499:
	s_add_u32 s20, s18, 0xf00
	s_addc_u32 s21, s19, 0
	s_and_b64 s[14:15], s[14:15], exec
	ds_write_b128 v137, v[0:3]
	s_cselect_b32 s14, s12, s20
	s_cselect_b32 s15, s13, s21
	s_add_u32 s43, s18, 0x100
	v_mov_b32_e32 v0, 0
	s_addc_u32 s44, s19, 0
	s_mov_b32 s45, -2
	s_mov_b64 s[18:19], 0
	v_mov_b32_e32 v1, v0
	v_mov_b32_e32 v2, v0
	v_mov_b32_e32 v3, v0
	v_mov_b32_e32 v4, v0
	v_mov_b32_e32 v5, v0
	v_mov_b32_e32 v6, v0
	v_mov_b32_e32 v7, v0
	v_mov_b32_e32 v16, v0
	v_mov_b32_e32 v17, v0
	v_mov_b32_e32 v18, v0
	v_mov_b32_e32 v19, v0
	v_mov_b32_e32 v24, v0
	v_mov_b32_e32 v25, v0
	v_mov_b32_e32 v26, v0
	v_mov_b32_e32 v27, v0
	v_mov_b32_e32 v32, v0
	v_mov_b32_e32 v33, v0
	v_mov_b32_e32 v34, v0
	v_mov_b32_e32 v35, v0
	v_mov_b32_e32 v40, v0
	v_mov_b32_e32 v41, v0
	v_mov_b32_e32 v42, v0
	v_mov_b32_e32 v43, v0
	v_mov_b32_e32 v44, v0
	v_mov_b32_e32 v45, v0
	v_mov_b32_e32 v46, v0
	v_mov_b32_e32 v47, v0
	v_mov_b32_e32 v52, v0
	v_mov_b32_e32 v53, v0
	v_mov_b32_e32 v54, v0
	v_mov_b32_e32 v55, v0
	v_mov_b32_e32 v12, v0
	v_mov_b32_e32 v13, v0
	v_mov_b32_e32 v14, v0
	v_mov_b32_e32 v15, v0
	v_mov_b32_e32 v20, v0
	v_mov_b32_e32 v21, v0
	v_mov_b32_e32 v22, v0
	v_mov_b32_e32 v23, v0
	v_mov_b32_e32 v28, v0
	v_mov_b32_e32 v29, v0
	v_mov_b32_e32 v30, v0
	v_mov_b32_e32 v31, v0
	v_mov_b32_e32 v36, v0
	v_mov_b32_e32 v37, v0
	v_mov_b32_e32 v38, v0
	v_mov_b32_e32 v39, v0
	v_mov_b32_e32 v48, v0
	v_mov_b32_e32 v49, v0
	v_mov_b32_e32 v50, v0
	v_mov_b32_e32 v51, v0
	v_mov_b32_e32 v56, v0
	v_mov_b32_e32 v57, v0
	v_mov_b32_e32 v58, v0
	v_mov_b32_e32 v59, v0
	v_mov_b32_e32 v60, v0
	v_mov_b32_e32 v61, v0
	v_mov_b32_e32 v62, v0
	v_mov_b32_e32 v63, v0
	v_mov_b32_e32 v64, v0
	v_mov_b32_e32 v65, v0
	v_mov_b32_e32 v66, v0
	v_mov_b32_e32 v67, v0
	v_mov_b32_e32 v68, v0
	v_mov_b32_e32 v69, v0
	v_mov_b32_e32 v70, v0
	v_mov_b32_e32 v71, v0
	v_mov_b32_e32 v72, v0
	v_mov_b32_e32 v73, v0
	v_mov_b32_e32 v74, v0
	v_mov_b32_e32 v75, v0
	v_mov_b32_e32 v80, v0
	v_mov_b32_e32 v81, v0
	v_mov_b32_e32 v82, v0
	v_mov_b32_e32 v83, v0
	v_mov_b32_e32 v88, v0
	v_mov_b32_e32 v89, v0
	v_mov_b32_e32 v90, v0
	v_mov_b32_e32 v91, v0
	v_mov_b32_e32 v92, v0
	v_mov_b32_e32 v93, v0
	v_mov_b32_e32 v94, v0
	v_mov_b32_e32 v95, v0
	v_mov_b32_e32 v96, v0
	v_mov_b32_e32 v97, v0
	v_mov_b32_e32 v98, v0
	v_mov_b32_e32 v99, v0
	v_mov_b32_e32 v104, v0
	v_mov_b32_e32 v105, v0
	v_mov_b32_e32 v106, v0
	v_mov_b32_e32 v107, v0
	v_mov_b32_e32 v108, v0
	v_mov_b32_e32 v109, v0
	v_mov_b32_e32 v110, v0
	v_mov_b32_e32 v111, v0
	v_mov_b32_e32 v76, v0
	v_mov_b32_e32 v77, v0
	v_mov_b32_e32 v78, v0
	v_mov_b32_e32 v79, v0
	v_mov_b32_e32 v84, v0
	v_mov_b32_e32 v85, v0
	v_mov_b32_e32 v86, v0
	v_mov_b32_e32 v87, v0
	v_mov_b32_e32 v100, v0
	v_mov_b32_e32 v101, v0
	v_mov_b32_e32 v102, v0
	v_mov_b32_e32 v103, v0
	v_mov_b32_e32 v112, v0
	v_mov_b32_e32 v113, v0
	v_mov_b32_e32 v114, v0
	v_mov_b32_e32 v115, v0
	v_mov_b32_e32 v116, v0
	v_mov_b32_e32 v117, v0
	v_mov_b32_e32 v118, v0
	v_mov_b32_e32 v119, v0
	v_mov_b32_e32 v120, v0
	v_mov_b32_e32 v121, v0
	v_mov_b32_e32 v122, v0
	v_mov_b32_e32 v123, v0
	v_mov_b32_e32 v124, v0
	v_mov_b32_e32 v125, v0
	v_mov_b32_e32 v126, v0
	v_mov_b32_e32 v127, v0
	v_mov_b32_e32 v128, v0
	v_mov_b32_e32 v129, v0
	v_mov_b32_e32 v130, v0
	v_mov_b32_e32 v131, v0
	s_branch .LBB0_501

.LBB0_801:
	v_and_b32_e32 v5, 15, v4
	s_add_i32 s0, 0, 0x21000
	v_or_b32_e32 v6, s53, v5
	v_lshl_add_u32 v253, v4, 4, s0
	v_and_b32_e32 v7, 48, v4
	v_lshlrev_b32_e32 v8, 6, v6
	s_movk_i32 s0, 0x3c0
	v_and_or_b32 v8, v8, s0, v7
	v_lshlrev_b32_e32 v4, 2, v4
	s_add_u32 s0, s18, 0x80
	v_lshl_or_b32 v5, v5, 6, v7
	v_and_b32_e32 v4, 32, v4
	s_addc_u32 s1, s19, 0
	v_bitop3_b32 v158, v5, s56, v4 bitop3:0xde
	s_waitcnt vmcnt(2)
	s_barrier
	s_add_i32 m0, s7, 0x18000
	v_lshl_add_u64 v[4:5], s[0:1], 0, v[140:141]
	global_load_lds_dwordx4 v[4:5], off
	s_add_i32 m0, s7, 0x1a000
	v_lshl_add_u64 v[4:5], s[0:1], 0, v[142:143]
	s_add_u32 s0, s90, 0x12800080
	s_addc_u32 s1, s91, 0
	s_add_i32 s60, s7, 0x8000
	global_load_lds_dwordx4 v[4:5], off
	s_mov_b32 m0, s60
	v_lshl_add_u64 v[4:5], s[0:1], 0, v[0:1]
	s_add_i32 s61, s7, 0xa000
	global_load_lds_dwordx4 v[4:5], off
	v_lshl_add_u64 v[4:5], s[0:1], 0, v[144:145]
	s_add_u32 s0, s18, 0x40080
	s_mov_b32 m0, s61
	s_addc_u32 s1, s19, 0
	global_load_lds_dwordx4 v[4:5], off
	s_add_i32 m0, s7, 0x1c000
	v_lshl_add_u64 v[4:5], s[0:1], 0, v[140:141]
	global_load_lds_dwordx4 v[4:5], off
	v_lshl_add_u64 v[4:5], s[0:1], 0, v[142:143]
	s_add_i32 m0, s7, 0x1e000
	v_lshlrev_b32_e32 v6, 2, v6
	global_load_lds_dwordx4 v[4:5], off
	v_and_b32_e32 v6, 32, v6
	s_waitcnt vmcnt(6)
	v_readlane_b32 s0, v255, 25
	v_bitop3_b32 v6, v8, s55, v6 bitop3:0xde
	s_cmpk_lt_u32 s0, 0x100
	s_cselect_b64 s[22:23], -1, 0
	s_add_i32 s62, 0, 0x10000
	s_add_i32 s63, 0, 0x14000
	v_add_u32_e32 v143, 0, v6
	v_mov_b32_e32 v145, 0x7f7f7f7f
	s_mov_b32 s24, 0x3c800000
	s_mov_b32 s64, 0xc0c00000
	v_mov_b32_e32 v159, 0x41000000
	v_mov_b32_e32 v4, v141
	v_mov_b32_e32 v5, v141
	v_mov_b32_e32 v6, v141
	v_mov_b32_e32 v7, v141
	v_mov_b32_e32 v8, v141
	v_mov_b32_e32 v9, v141
	v_mov_b32_e32 v10, v141
	v_mov_b32_e32 v11, v141
	v_mov_b32_e32 v12, v141
	v_mov_b32_e32 v13, v141
	v_mov_b32_e32 v14, v141
	v_mov_b32_e32 v15, v141
	v_mov_b32_e32 v16, v141
	v_mov_b32_e32 v17, v141
	v_mov_b32_e32 v18, v141
	v_mov_b32_e32 v19, v141
	v_mov_b32_e32 v20, v141
	v_mov_b32_e32 v21, v141
	v_mov_b32_e32 v22, v141
	v_mov_b32_e32 v23, v141
	v_mov_b32_e32 v24, v141
	v_mov_b32_e32 v25, v141
	v_mov_b32_e32 v26, v141
	v_mov_b32_e32 v27, v141
	v_mov_b32_e32 v232, v141
	v_mov_b32_e32 v233, v141
	v_mov_b32_e32 v234, v141
	v_mov_b32_e32 v235, v141
	v_mov_b32_e32 v32, v141
	v_mov_b32_e32 v33, v141
	v_mov_b32_e32 v34, v141
	v_mov_b32_e32 v35, v141
	v_mov_b32_e32 v36, v141
	v_mov_b32_e32 v37, v141
	v_mov_b32_e32 v38, v141
	v_mov_b32_e32 v39, v141
	v_mov_b32_e32 v40, v141
	v_mov_b32_e32 v41, v141
	v_mov_b32_e32 v42, v141
	v_mov_b32_e32 v43, v141
	v_mov_b32_e32 v44, v141
	v_mov_b32_e32 v45, v141
	v_mov_b32_e32 v46, v141
	v_mov_b32_e32 v47, v141
	v_mov_b32_e32 v48, v141
	v_mov_b32_e32 v49, v141
	v_mov_b32_e32 v50, v141
	v_mov_b32_e32 v51, v141
	v_mov_b32_e32 v52, v141
	v_mov_b32_e32 v53, v141
	v_mov_b32_e32 v54, v141
	v_mov_b32_e32 v55, v141
	v_mov_b32_e32 v56, v141
	v_mov_b32_e32 v57, v141
	v_mov_b32_e32 v58, v141
	v_mov_b32_e32 v59, v141
	v_mov_b32_e32 v60, v141
	v_mov_b32_e32 v61, v141
	v_mov_b32_e32 v62, v141
	v_mov_b32_e32 v63, v141
	v_mov_b32_e32 v64, v141
	v_mov_b32_e32 v65, v141
	v_mov_b32_e32 v66, v141
	v_mov_b32_e32 v67, v141
	v_mov_b32_e32 v28, v141
	v_mov_b32_e32 v29, v141
	v_mov_b32_e32 v30, v141
	v_mov_b32_e32 v31, v141
	v_mov_b32_e32 v72, v141
	v_mov_b32_e32 v73, v141
	v_mov_b32_e32 v74, v141
	v_mov_b32_e32 v75, v141
	v_mov_b32_e32 v76, v141
	v_mov_b32_e32 v77, v141
	v_mov_b32_e32 v78, v141
	v_mov_b32_e32 v79, v141
	v_mov_b32_e32 v80, v141
	v_mov_b32_e32 v81, v141
	v_mov_b32_e32 v82, v141
	v_mov_b32_e32 v83, v141
	v_mov_b32_e32 v84, v141
	v_mov_b32_e32 v85, v141
	v_mov_b32_e32 v86, v141
	v_mov_b32_e32 v87, v141
	v_mov_b32_e32 v88, v141
	v_mov_b32_e32 v89, v141
	v_mov_b32_e32 v90, v141
	v_mov_b32_e32 v91, v141
	v_mov_b32_e32 v92, v141
	v_mov_b32_e32 v93, v141
	v_mov_b32_e32 v94, v141
	v_mov_b32_e32 v95, v141
	v_mov_b32_e32 v96, v141
	v_mov_b32_e32 v97, v141
	v_mov_b32_e32 v98, v141
	v_mov_b32_e32 v99, v141
	v_mov_b32_e32 v100, v141
	v_mov_b32_e32 v101, v141
	v_mov_b32_e32 v102, v141
	v_mov_b32_e32 v103, v141
	v_mov_b32_e32 v104, v141
	v_mov_b32_e32 v105, v141
	v_mov_b32_e32 v106, v141
	v_mov_b32_e32 v107, v141
	v_mov_b32_e32 v108, v141
	v_mov_b32_e32 v109, v141
	v_mov_b32_e32 v110, v141
	v_mov_b32_e32 v111, v141
	v_mov_b32_e32 v112, v141
	v_mov_b32_e32 v113, v141
	v_mov_b32_e32 v114, v141
	v_mov_b32_e32 v115, v141
	v_mov_b32_e32 v116, v141
	v_mov_b32_e32 v117, v141
	v_mov_b32_e32 v118, v141
	v_mov_b32_e32 v119, v141
	v_mov_b32_e32 v120, v141
	v_mov_b32_e32 v121, v141
	v_mov_b32_e32 v122, v141
	v_mov_b32_e32 v123, v141
	v_mov_b32_e32 v124, v141
	v_mov_b32_e32 v125, v141
	v_mov_b32_e32 v126, v141
	v_mov_b32_e32 v127, v141
	v_mov_b32_e32 v128, v141
	v_mov_b32_e32 v129, v141
	v_mov_b32_e32 v130, v141
	v_mov_b32_e32 v131, v141
	s_barrier
	s_branch .LBB0_804

.LBB0_886:
	v_and_b32_e32 v5, 15, v4
	s_add_i32 s0, 0, 0x21000
	v_or_b32_e32 v6, s53, v5
	v_lshl_add_u32 v253, v4, 4, s0
	v_and_b32_e32 v7, 48, v4
	v_lshlrev_b32_e32 v8, 6, v6
	s_movk_i32 s0, 0x3c0
	v_and_or_b32 v8, v8, s0, v7
	v_lshlrev_b32_e32 v4, 2, v4
	s_add_u32 s0, s18, 0x80
	v_lshl_or_b32 v5, v5, 6, v7
	v_and_b32_e32 v4, 32, v4
	s_addc_u32 s1, s19, 0
	v_bitop3_b32 v158, v5, s56, v4 bitop3:0xde
	s_waitcnt vmcnt(2)
	s_barrier
	s_add_i32 m0, s7, 0x18000
	v_lshl_add_u64 v[4:5], s[0:1], 0, v[140:141]
	v_lshlrev_b32_e32 v6, 2, v6
	global_load_lds_dwordx4 v[4:5], off
	s_add_i32 m0, s7, 0x1a000
	v_and_b32_e32 v6, 32, v6
	v_lshl_add_u64 v[4:5], s[0:1], 0, v[142:143]
	s_add_u32 s0, s90, 0x12800080
	v_bitop3_b32 v6, v8, s55, v6 bitop3:0xde
	s_addc_u32 s1, s91, 0
	s_add_i32 s55, s7, 0x8000
	global_load_lds_dwordx4 v[4:5], off
	s_mov_b32 m0, s55
	v_lshl_add_u64 v[4:5], s[0:1], 0, v[0:1]
	s_add_i32 s56, s7, 0xa000
	global_load_lds_dwordx4 v[4:5], off
	v_lshl_add_u64 v[4:5], s[0:1], 0, v[144:145]
	s_add_u32 s0, s18, 0x40080
	s_mov_b32 m0, s56
	s_addc_u32 s1, s19, 0
	global_load_lds_dwordx4 v[4:5], off
	s_add_i32 m0, s7, 0x1c000
	v_lshl_add_u64 v[4:5], s[0:1], 0, v[140:141]
	global_load_lds_dwordx4 v[4:5], off
	v_lshl_add_u64 v[4:5], s[0:1], 0, v[142:143]
	s_add_i32 m0, s7, 0x1e000
	v_readlane_b32 s0, v255, 25
	global_load_lds_dwordx4 v[4:5], off
	s_waitcnt vmcnt(6)
	s_cmpk_lt_u32 s0, 0x100
	s_cselect_b64 s[22:23], -1, 0
	s_add_i32 s57, 0, 0x10000
	s_add_i32 s61, 0, 0x14000
	v_add_u32_e32 v143, 0, v6
	v_mov_b32_e32 v145, 0x7f7f7f7f
	s_mov_b32 s24, 0x3c800000
	s_mov_b32 s62, 0xc0c00000
	s_mov_b32 s63, 0x40000
	v_mov_b32_e32 v159, 0x41000000
	v_mov_b32_e32 v4, v141
	v_mov_b32_e32 v5, v141
	v_mov_b32_e32 v6, v141
	v_mov_b32_e32 v7, v141
	v_mov_b32_e32 v8, v141
	v_mov_b32_e32 v9, v141
	v_mov_b32_e32 v10, v141
	v_mov_b32_e32 v11, v141
	v_mov_b32_e32 v12, v141
	v_mov_b32_e32 v13, v141
	v_mov_b32_e32 v14, v141
	v_mov_b32_e32 v15, v141
	v_mov_b32_e32 v16, v141
	v_mov_b32_e32 v17, v141
	v_mov_b32_e32 v18, v141
	v_mov_b32_e32 v19, v141
	v_mov_b32_e32 v20, v141
	v_mov_b32_e32 v21, v141
	v_mov_b32_e32 v22, v141
	v_mov_b32_e32 v23, v141
	v_mov_b32_e32 v24, v141
	v_mov_b32_e32 v25, v141
	v_mov_b32_e32 v26, v141
	v_mov_b32_e32 v27, v141
	v_mov_b32_e32 v232, v141
	v_mov_b32_e32 v233, v141
	v_mov_b32_e32 v234, v141
	v_mov_b32_e32 v235, v141
	v_mov_b32_e32 v32, v141
	v_mov_b32_e32 v33, v141
	v_mov_b32_e32 v34, v141
	v_mov_b32_e32 v35, v141
	v_mov_b32_e32 v36, v141
	v_mov_b32_e32 v37, v141
	v_mov_b32_e32 v38, v141
	v_mov_b32_e32 v39, v141
	v_mov_b32_e32 v40, v141
	v_mov_b32_e32 v41, v141
	v_mov_b32_e32 v42, v141
	v_mov_b32_e32 v43, v141
	v_mov_b32_e32 v44, v141
	v_mov_b32_e32 v45, v141
	v_mov_b32_e32 v46, v141
	v_mov_b32_e32 v47, v141
	v_mov_b32_e32 v48, v141
	v_mov_b32_e32 v49, v141
	v_mov_b32_e32 v50, v141
	v_mov_b32_e32 v51, v141
	v_mov_b32_e32 v52, v141
	v_mov_b32_e32 v53, v141
	v_mov_b32_e32 v54, v141
	v_mov_b32_e32 v55, v141
	v_mov_b32_e32 v56, v141
	v_mov_b32_e32 v57, v141
	v_mov_b32_e32 v58, v141
	v_mov_b32_e32 v59, v141
	v_mov_b32_e32 v60, v141
	v_mov_b32_e32 v61, v141
	v_mov_b32_e32 v62, v141
	v_mov_b32_e32 v63, v141
	v_mov_b32_e32 v64, v141
	v_mov_b32_e32 v65, v141
	v_mov_b32_e32 v66, v141
	v_mov_b32_e32 v67, v141
	v_mov_b32_e32 v28, v141
	v_mov_b32_e32 v29, v141
	v_mov_b32_e32 v30, v141
	v_mov_b32_e32 v31, v141
	v_mov_b32_e32 v72, v141
	v_mov_b32_e32 v73, v141
	v_mov_b32_e32 v74, v141
	v_mov_b32_e32 v75, v141
	v_mov_b32_e32 v76, v141
	v_mov_b32_e32 v77, v141
	v_mov_b32_e32 v78, v141
	v_mov_b32_e32 v79, v141
	v_mov_b32_e32 v80, v141
	v_mov_b32_e32 v81, v141
	v_mov_b32_e32 v82, v141
	v_mov_b32_e32 v83, v141
	v_mov_b32_e32 v84, v141
	v_mov_b32_e32 v85, v141
	v_mov_b32_e32 v86, v141
	v_mov_b32_e32 v87, v141
	v_mov_b32_e32 v88, v141
	v_mov_b32_e32 v89, v141
	v_mov_b32_e32 v90, v141
	v_mov_b32_e32 v91, v141
	v_mov_b32_e32 v92, v141
	v_mov_b32_e32 v93, v141
	v_mov_b32_e32 v94, v141
	v_mov_b32_e32 v95, v141
	v_mov_b32_e32 v96, v141
	v_mov_b32_e32 v97, v141
	v_mov_b32_e32 v98, v141
	v_mov_b32_e32 v99, v141
	v_mov_b32_e32 v100, v141
	v_mov_b32_e32 v101, v141
	v_mov_b32_e32 v102, v141
	v_mov_b32_e32 v103, v141
	v_mov_b32_e32 v104, v141
	v_mov_b32_e32 v105, v141
	v_mov_b32_e32 v106, v141
	v_mov_b32_e32 v107, v141
	v_mov_b32_e32 v108, v141
	v_mov_b32_e32 v109, v141
	v_mov_b32_e32 v110, v141
	v_mov_b32_e32 v111, v141
	v_mov_b32_e32 v112, v141
	v_mov_b32_e32 v113, v141
	v_mov_b32_e32 v114, v141
	v_mov_b32_e32 v115, v141
	v_mov_b32_e32 v116, v141
	v_mov_b32_e32 v117, v141
	v_mov_b32_e32 v118, v141
	v_mov_b32_e32 v119, v141
	v_mov_b32_e32 v120, v141
	v_mov_b32_e32 v121, v141
	v_mov_b32_e32 v122, v141
	v_mov_b32_e32 v123, v141
	v_mov_b32_e32 v124, v141
	v_mov_b32_e32 v125, v141
	v_mov_b32_e32 v126, v141
	v_mov_b32_e32 v127, v141
	v_mov_b32_e32 v128, v141
	v_mov_b32_e32 v129, v141
	v_mov_b32_e32 v130, v141
	v_mov_b32_e32 v131, v141
	s_barrier
	s_branch .LBB0_889

.LBB0_1031:
	s_add_i32 s16, 0, 0x21000
	v_lshl_add_u32 v252, v4, 4, s16
	s_add_u32 s16, s90, 0x1e800000
	v_and_b32_e32 v5, 48, v4
	v_lshlrev_b32_e32 v6, 6, v4
	s_movk_i32 s19, 0x3c0
	v_lshlrev_b32_e32 v4, 2, v4
	s_addc_u32 s17, s91, 0
	s_lshl_b32 s53, s18, 6
	s_lshl_b32 s18, s18, 13
	v_and_or_b32 v5, v6, s19, v5
	v_and_b32_e32 v4, 32, v4
	v_bitop3_b32 v6, v5, s18, v4 bitop3:0xde
	s_lshl_b32 s18, s94, 5
	s_and_b32 s55, s18, 0x60
	s_lshl_b32 s18, s55, 7
	v_bitop3_b32 v158, v5, s18, v4 bitop3:0xde
	s_add_u32 s18, s12, 0x80
	s_addc_u32 s19, s13, 0
	s_waitcnt vmcnt(2)
	s_barrier
	s_add_i32 m0, s1, 0x18000
	v_lshl_add_u64 v[4:5], s[18:19], 0, v[148:149]
	global_load_lds_dwordx4 v[4:5], off
	s_add_i32 m0, s1, 0x1a000
	v_lshl_add_u64 v[4:5], s[18:19], 0, v[150:151]
	s_add_u32 s18, s90, 0x14800080
	s_addc_u32 s19, s91, 0
	s_add_i32 s56, s1, 0x8000
	global_load_lds_dwordx4 v[4:5], off
	s_mov_b32 m0, s56
	v_lshl_add_u64 v[4:5], s[18:19], 0, v[0:1]
	s_add_i32 s57, s1, 0xa000
	global_load_lds_dwordx4 v[4:5], off
	v_lshl_add_u64 v[4:5], s[18:19], 0, v[152:153]
	s_add_u32 s18, s12, 0x40080
	s_mov_b32 m0, s57
	s_addc_u32 s19, s13, 0
	global_load_lds_dwordx4 v[4:5], off
	s_add_i32 m0, s1, 0x1c000
	v_lshl_add_u64 v[4:5], s[18:19], 0, v[148:149]
	global_load_lds_dwordx4 v[4:5], off
	v_lshl_add_u64 v[4:5], s[18:19], 0, v[150:151]
	s_add_i32 m0, s1, 0x1e000
	v_readlane_b32 s18, v255, 25
	global_load_lds_dwordx4 v[4:5], off
	s_waitcnt vmcnt(6)
	s_cmpk_lt_u32 s18, 0x100
	s_cselect_b64 s[18:19], -1, 0
	s_add_i32 s58, 0, 0x10000
	s_add_i32 s59, 0, 0x14000
	v_add_u32_e32 v151, 0, v6
	v_mov_b32_e32 v153, 0x7f7f7f7f
	s_mov_b32 s20, 0x3c800000
	s_mov_b32 s60, 0x40000
	s_mov_b32 s61, 0x50000
	s_mov_b32 s22, s0
	v_mov_b32_e32 v4, v149
	v_mov_b32_e32 v5, v149
	v_mov_b32_e32 v6, v149
	v_mov_b32_e32 v7, v149
	v_mov_b32_e32 v8, v149
	v_mov_b32_e32 v9, v149
	v_mov_b32_e32 v10, v149
	v_mov_b32_e32 v11, v149
	v_mov_b32_e32 v12, v149
	v_mov_b32_e32 v13, v149
	v_mov_b32_e32 v14, v149
	v_mov_b32_e32 v15, v149
	v_mov_b32_e32 v16, v149
	v_mov_b32_e32 v17, v149
	v_mov_b32_e32 v18, v149
	v_mov_b32_e32 v19, v149
	v_mov_b32_e32 v20, v149
	v_mov_b32_e32 v21, v149
	v_mov_b32_e32 v22, v149
	v_mov_b32_e32 v23, v149
	v_mov_b32_e32 v24, v149
	v_mov_b32_e32 v25, v149
	v_mov_b32_e32 v26, v149
	v_mov_b32_e32 v27, v149
	v_mov_b32_e32 v232, v149
	v_mov_b32_e32 v233, v149
	v_mov_b32_e32 v234, v149
	v_mov_b32_e32 v235, v149
	v_mov_b32_e32 v32, v149
	v_mov_b32_e32 v33, v149
	v_mov_b32_e32 v34, v149
	v_mov_b32_e32 v35, v149
	v_mov_b32_e32 v36, v149
	v_mov_b32_e32 v37, v149
	v_mov_b32_e32 v38, v149
	v_mov_b32_e32 v39, v149
	v_mov_b32_e32 v40, v149
	v_mov_b32_e32 v41, v149
	v_mov_b32_e32 v42, v149
	v_mov_b32_e32 v43, v149
	v_mov_b32_e32 v44, v149
	v_mov_b32_e32 v45, v149
	v_mov_b32_e32 v46, v149
	v_mov_b32_e32 v47, v149
	v_mov_b32_e32 v48, v149
	v_mov_b32_e32 v49, v149
	v_mov_b32_e32 v50, v149
	v_mov_b32_e32 v51, v149
	v_mov_b32_e32 v52, v149
	v_mov_b32_e32 v53, v149
	v_mov_b32_e32 v54, v149
	v_mov_b32_e32 v55, v149
	v_mov_b32_e32 v56, v149
	v_mov_b32_e32 v57, v149
	v_mov_b32_e32 v58, v149
	v_mov_b32_e32 v59, v149
	v_mov_b32_e32 v60, v149
	v_mov_b32_e32 v61, v149
	v_mov_b32_e32 v62, v149
	v_mov_b32_e32 v63, v149
	v_mov_b32_e32 v64, v149
	v_mov_b32_e32 v65, v149
	v_mov_b32_e32 v66, v149
	v_mov_b32_e32 v67, v149
	v_mov_b32_e32 v28, v149
	v_mov_b32_e32 v29, v149
	v_mov_b32_e32 v30, v149
	v_mov_b32_e32 v31, v149
	v_mov_b32_e32 v72, v149
	v_mov_b32_e32 v73, v149
	v_mov_b32_e32 v74, v149
	v_mov_b32_e32 v75, v149
	v_mov_b32_e32 v76, v149
	v_mov_b32_e32 v77, v149
	v_mov_b32_e32 v78, v149
	v_mov_b32_e32 v79, v149
	v_mov_b32_e32 v80, v149
	v_mov_b32_e32 v81, v149
	v_mov_b32_e32 v82, v149
	v_mov_b32_e32 v83, v149
	v_mov_b32_e32 v84, v149
	v_mov_b32_e32 v85, v149
	v_mov_b32_e32 v86, v149
	v_mov_b32_e32 v87, v149
	v_mov_b32_e32 v88, v149
	v_mov_b32_e32 v89, v149
	v_mov_b32_e32 v90, v149
	v_mov_b32_e32 v91, v149
	v_mov_b32_e32 v92, v149
	v_mov_b32_e32 v93, v149
	v_mov_b32_e32 v94, v149
	v_mov_b32_e32 v95, v149
	v_mov_b32_e32 v96, v149
	v_mov_b32_e32 v97, v149
	v_mov_b32_e32 v98, v149
	v_mov_b32_e32 v99, v149
	v_mov_b32_e32 v100, v149
	v_mov_b32_e32 v101, v149
	v_mov_b32_e32 v102, v149
	v_mov_b32_e32 v103, v149
	v_mov_b32_e32 v104, v149
	v_mov_b32_e32 v105, v149
	v_mov_b32_e32 v106, v149
	v_mov_b32_e32 v107, v149
	v_mov_b32_e32 v108, v149
	v_mov_b32_e32 v109, v149
	v_mov_b32_e32 v110, v149
	v_mov_b32_e32 v111, v149
	v_mov_b32_e32 v112, v149
	v_mov_b32_e32 v113, v149
	v_mov_b32_e32 v114, v149
	v_mov_b32_e32 v115, v149
	v_mov_b32_e32 v116, v149
	v_mov_b32_e32 v117, v149
	v_mov_b32_e32 v118, v149
	v_mov_b32_e32 v119, v149
	v_mov_b32_e32 v120, v149
	v_mov_b32_e32 v121, v149
	v_mov_b32_e32 v122, v149
	v_mov_b32_e32 v123, v149
	v_mov_b32_e32 v124, v149
	v_mov_b32_e32 v125, v149
	v_mov_b32_e32 v126, v149
	v_mov_b32_e32 v127, v149
	v_mov_b32_e32 v128, v149
	v_mov_b32_e32 v129, v149
	v_mov_b32_e32 v130, v149
	v_mov_b32_e32 v131, v149
	s_barrier
	s_branch .LBB0_1034
